# attention tile loops: 104 dead SGPR-tuple restores (v_readlane whose SGPR is never read before being redefined) removed from the DMA-issue branches
# baseline (speedup 1.0000x reference)
.LBB0_1582:
	s_add_i32 s19, s88, s14
	v_cndmask_b32_e64 v36, 0, 1, s[82:83]
	s_add_i32 s79, s19, -2
	v_cmp_ne_u32_e64 s[40:41], 1, v36
	s_andn2_b64 vcc, exec, s[82:83]
	s_mov_b64 s[8:9], -1
	s_cbranch_vccnz .LBB0_1594
	s_mov_b64 s[8:9], 0
	s_andn2_b64 vcc, exec, s[42:43]
	s_mov_b64 s[6:7], 0
	s_mov_b32 s89, s31
	s_cbranch_vccnz .LBB0_1594
	s_bfe_u32 s4, s79, 0x10001
	s_or_b32 s22, s4, s13
	s_cmp_ge_i32 s31, s81
	s_cbranch_scc1 .LBB0_1589
	s_mul_hi_i32 s4, s31, 0x2aaaaaab
	s_lshr_b32 s6, s4, 31
	s_ashr_i32 s4, s4, 5
	s_add_i32 s4, s4, s6
	v_readlane_b32 s6, v255, 24
	s_add_i32 s89, s4, s6
	s_mulk_i32 s4, 0xc0
	s_sub_i32 s4, s31, s4
	s_cmpk_lt_i32 s4, 0x80
	s_cselect_b32 s6, s33, s23
	s_add_i32 s28, s4, s6
	s_bfe_u32 s84, s28, 0x30004
	s_lshl_b32 s6, s28, 6
	s_ashr_i32 s77, s28, 7
	s_lshl_b32 s59, s89, 5
	s_and_b32 s85, s6, 0x3c0
	s_lshl_b32 s58, s84, 5
	v_readlane_b32 s7, v255, 25
	s_cmpk_gt_i32 s4, 0x7f
	s_mov_b64 s[10:11], -1
	s_cbranch_scc0 .LBB0_1587
	s_ashr_i32 s4, s28, 9
	s_add_i32 s6, s4, s59
	s_ashr_i32 s7, s6, 31
	s_lshl_b64 s[6:7], s[6:7], 22
	v_readlane_b32 s72, v252, 2
	v_readlane_b32 s73, v252, 3
	s_add_u32 s4, s72, s6
	s_addc_u32 s7, s73, s7
	s_lshl_b32 s6, s85, 12
	s_add_u32 s6, s4, s6
	s_addc_u32 s7, s7, 0
	s_lshl_b32 s4, s77, 8
	s_and_b32 s4, s4, 0x300
	v_readlane_b32 s64, v251, 58
	v_readlane_b32 s65, v251, 59
	s_or_b32 s4, s58, s4
	s_mov_b64 s[10:11], 0
.LBB0_1587:
	s_andn2_b64 vcc, exec, s[10:11]
	s_cbranch_vccnz .LBB0_1590
	s_ashr_i32 s4, s28, 10
	s_add_i32 s6, s4, s59
	s_ashr_i32 s7, s6, 31
	s_lshl_b64 s[6:7], s[6:7], 23
	v_readlane_b32 s68, v251, 62
	v_readlane_b32 s69, v251, 63
	s_add_u32 s4, s68, s6
	s_addc_u32 s7, s69, s7
	s_lshl_b32 s6, s85, 13
	s_add_u32 s6, s4, s6
	s_addc_u32 s7, s7, 0
	s_lshl_b32 s10, s84, 8
	s_and_b32 s10, s10, 0x400
	s_and_b32 s11, s28, 0x380
	s_and_b32 s4, s58, 0x60
	s_or_b32 s10, s10, s11
	s_mov_b32 s58, 8
	s_or_b32 s4, s10, s4
	s_movk_i32 s28, 0x800
	s_mov_b64 s[10:11], 0x1d08000
	v_readlane_b32 s64, v251, 58
	v_readlane_b32 s65, v251, 59
	s_branch .LBB0_1591

.LBB0_1620:
	s_andn2_b64 vcc, exec, s[42:43]
	s_cbranch_vccnz .LBB0_1631
	s_add_i32 s19, s19, -1
	s_bfe_u32 s6, s19, 0x10001
	s_or_b32 s10, s6, s13
	s_mov_b32 s4, -1
	s_cmp_ge_i32 s89, s81
	s_mov_b64 s[6:7], 0
	s_cbranch_scc1 .LBB0_1628
	s_mul_hi_i32 s4, s89, 0x2aaaaaab
	s_lshr_b32 s6, s4, 31
	s_ashr_i32 s4, s4, 5
	s_add_i32 s4, s4, s6
	v_readlane_b32 s6, v255, 24
	s_add_i32 s28, s4, s6
	s_mulk_i32 s4, 0xc0
	s_sub_i32 s4, s89, s4
	s_cmpk_lt_i32 s4, 0x80
	s_cselect_b32 s6, s33, s23
	s_add_i32 s11, s4, s6
	s_bfe_u32 s19, s11, 0x30004
	s_lshl_b32 s6, s11, 6
	s_ashr_i32 s31, s11, 7
	s_lshl_b32 s41, s28, 5
	s_and_b32 s22, s6, 0x3c0
	s_lshl_b32 s40, s19, 5
	v_readlane_b32 s7, v255, 25
	s_cmpk_gt_i32 s4, 0x7f
	s_mov_b64 s[8:9], -1
	s_cbranch_scc0 .LBB0_1624
	s_ashr_i32 s4, s11, 9
	s_add_i32 s6, s4, s41
	s_ashr_i32 s7, s6, 31
	s_lshl_b64 s[6:7], s[6:7], 22
	v_readlane_b32 s72, v252, 2
	v_readlane_b32 s73, v252, 3
	s_add_u32 s4, s72, s6
	s_addc_u32 s7, s73, s7
	s_lshl_b32 s6, s22, 12
	s_add_u32 s6, s4, s6
	s_addc_u32 s7, s7, 0
	s_lshl_b32 s4, s31, 8
	s_and_b32 s4, s4, 0x300
	v_readlane_b32 s64, v251, 58
	v_readlane_b32 s65, v251, 59
	s_or_b32 s4, s40, s4
	s_mov_b64 s[8:9], 0
.LBB0_1624:
	s_andn2_b64 vcc, exec, s[8:9]
	s_cbranch_vccnz .LBB0_1626
	s_ashr_i32 s4, s11, 10
	s_add_i32 s6, s4, s41
	s_ashr_i32 s7, s6, 31
	s_lshl_b64 s[6:7], s[6:7], 23
	v_readlane_b32 s68, v251, 62
	v_readlane_b32 s69, v251, 63
	s_add_u32 s4, s68, s6
	s_addc_u32 s7, s69, s7
	s_lshl_b32 s6, s22, 13
	s_add_u32 s6, s4, s6
	s_addc_u32 s7, s7, 0
	s_lshl_b32 s8, s19, 8
	s_and_b32 s8, s8, 0x400
	s_and_b32 s9, s11, 0x380
	s_and_b32 s4, s40, 0x60
	s_or_b32 s8, s8, s9
	s_mov_b32 s40, 8
	s_or_b32 s4, s8, s4
	s_movk_i32 s11, 0x800
	s_mov_b64 s[8:9], 0x1d08000
	v_readlane_b32 s64, v251, 58
	v_readlane_b32 s65, v251, 59
	s_branch .LBB0_1627

.LBB0_1987:
	s_add_i32 s12, s83, s76
	v_cndmask_b32_e64 v86, 0, 1, s[44:45]
	s_add_i32 s55, s12, -2
	v_cmp_ne_u32_e64 s[40:41], 1, v86
	s_andn2_b64 vcc, exec, s[44:45]
	s_mov_b64 s[48:49], -1
	s_cbranch_vccnz .LBB0_1999
	s_mov_b64 s[48:49], 0
	s_andn2_b64 vcc, exec, s[16:17]
	s_mov_b64 s[46:47], 0
	s_mov_b32 s13, s88
	s_cbranch_vccnz .LBB0_1999
	s_bfe_u32 s4, s55, 0x10001
	s_or_b32 s22, s4, s3
	s_cmp_ge_i32 s88, s54
	s_cbranch_scc1 .LBB0_1994
	s_mul_hi_i32 s4, s88, 0x2aaaaaab
	s_lshr_b32 s13, s4, 31
	s_ashr_i32 s63, s4, 5
	s_add_i32 s8, s63, s13
	s_mul_i32 s4, s8, 0xc0
	s_sub_i32 s4, s88, s4
	s_cmpk_lt_i32 s4, 0x80
	s_cselect_b32 s13, s33, s23
	s_add_i32 s13, s4, s13
	s_bfe_u32 s28, s13, 0x30004
	s_lshl_b32 s46, s13, 6
	s_ashr_i32 s78, s13, 7
	s_lshl_b32 s58, s8, 5
	s_and_b32 s15, s46, 0x3c0
	s_lshl_b32 s77, s28, 5
	s_cmpk_gt_i32 s4, 0x7f
	s_mov_b64 s[50:51], -1
	s_cbranch_scc0 .LBB0_1992
	s_ashr_i32 s4, s13, 9
	s_add_i32 s46, s4, s58
	s_ashr_i32 s47, s46, 31
	s_lshl_b64 s[46:47], s[46:47], 22
	v_readlane_b32 s72, v252, 2
	v_readlane_b32 s73, v252, 3
	s_add_u32 s4, s72, s46
	s_addc_u32 s47, s73, s47
	s_lshl_b32 s46, s15, 12
	s_add_u32 s46, s4, s46
	s_addc_u32 s47, s47, 0
	s_lshl_b32 s4, s78, 8
	s_and_b32 s4, s4, 0x300
	s_or_b32 s4, s77, s4
	s_mov_b64 s[50:51], 0
.LBB0_1992:
	s_andn2_b64 vcc, exec, s[50:51]
	s_cbranch_vccnz .LBB0_1995
	s_ashr_i32 s4, s13, 10
	s_add_i32 s46, s4, s58
	s_ashr_i32 s47, s46, 31
	s_lshl_b64 s[46:47], s[46:47], 23
	v_readlane_b32 s68, v251, 62
	v_readlane_b32 s69, v251, 63
	s_add_u32 s4, s68, s46
	s_addc_u32 s47, s69, s47
	s_lshl_b32 s46, s15, 13
	s_add_u32 s46, s4, s46
	s_addc_u32 s47, s47, 0
	s_lshl_b32 s50, s28, 8
	s_and_b32 s50, s50, 0x400
	s_and_b32 s13, s13, 0x380
	s_and_b32 s4, s77, 0x60
	s_or_b32 s13, s50, s13
	s_mov_b32 s58, 8
	s_or_b32 s4, s13, s4
	s_movk_i32 s13, 0x800
	s_mov_b64 s[50:51], 0x1d08000
	s_branch .LBB0_1996

.LBB0_2030:
	s_andn2_b64 vcc, exec, s[16:17]
	s_cbranch_vccnz .LBB0_2041
	s_add_i32 s12, s12, -1
	s_bfe_u32 s12, s12, 0x10001
	s_or_b32 s12, s12, s3
	s_mov_b32 s4, -1
	s_cmp_ge_i32 s13, s54
	s_cbranch_scc1 .LBB0_2038
	s_mul_hi_i32 s4, s13, 0x2aaaaaab
	s_lshr_b32 s22, s4, 31
	s_ashr_i32 s46, s4, 5
	s_add_i32 s46, s46, s22
	s_mul_i32 s4, s46, 0xc0
	s_sub_i32 s4, s13, s4
	s_cmpk_lt_i32 s4, 0x80
	s_cselect_b32 s22, s33, s23
	s_add_i32 s22, s4, s22
	s_bfe_u32 s28, s22, 0x30004
	s_lshl_b32 s31, s22, 6
	s_ashr_i32 s47, s22, 7
	s_lshl_b32 s49, s46, 5
	s_and_b32 s31, s31, 0x3c0
	s_lshl_b32 s48, s28, 5
	s_cmpk_gt_i32 s4, 0x7f
	s_mov_b64 s[40:41], -1
	s_cbranch_scc0 .LBB0_2034
	s_ashr_i32 s4, s22, 9
	s_add_i32 s38, s4, s49
	s_ashr_i32 s39, s38, 31
	s_lshl_b64 s[38:39], s[38:39], 22
	v_readlane_b32 s72, v252, 2
	v_readlane_b32 s73, v252, 3
	s_add_u32 s4, s72, s38
	s_addc_u32 s39, s73, s39
	s_lshl_b32 s38, s31, 12
	s_add_u32 s38, s4, s38
	s_addc_u32 s39, s39, 0
	s_lshl_b32 s4, s47, 8
	s_and_b32 s4, s4, 0x300
	s_or_b32 s4, s48, s4
	s_mov_b64 s[40:41], 0
.LBB0_2034:
	s_andn2_b64 vcc, exec, s[40:41]
	s_cbranch_vccnz .LBB0_2036
	s_ashr_i32 s4, s22, 10
	s_add_i32 s38, s4, s49
	s_ashr_i32 s39, s38, 31
	s_lshl_b64 s[38:39], s[38:39], 23
	v_readlane_b32 s68, v251, 62
	v_readlane_b32 s69, v251, 63
	s_add_u32 s4, s68, s38
	s_addc_u32 s39, s69, s39
	s_lshl_b32 s38, s31, 13
	s_add_u32 s38, s4, s38
	s_addc_u32 s39, s39, 0
	s_lshl_b32 s40, s28, 8
	s_and_b32 s40, s40, 0x400
	s_and_b32 s22, s22, 0x380
	s_and_b32 s4, s48, 0x60
	s_or_b32 s22, s40, s22
	s_mov_b32 s48, 8
	s_or_b32 s4, s22, s4
	s_movk_i32 s22, 0x800
	s_mov_b64 s[40:41], 0x1d08000
	s_branch .LBB0_2037
